# 96 helpers in both layer-0 MoE phases, all layer-1 items except the first 2048 deferred, nt helper stores
# speedup vs baseline: 1.0199x; 1.0070x over previous
;     ...
;         int it = gw; TrDesc dA, dB; f32x4 vA[16], vB[16];
;         if (it < NIT) { dA = decode(NIT - 1 - it); tr_load(dA, vA); }
;         while (it < NIT) {
;             const int itB = it + NGW;
;             if (itB < NIT) { dB = decode(NIT - 1 - itB); tr_load(dB, vB); }
;             tr_finish(dA, vA, scr, lane);
;             if (itB >= NIT) break;
;             const int itA = itB + NGW;
;             if (itA < NIT) { dA = decode(NIT - 1 - itA); tr_load(dA, vA); }
;             tr_finish(dB, vB, scr, lane);
;             it = itA;
;         }
.LBB0_72:
	s_cmp_gt_i32 s42, 0xfcff
	s_cbranch_scc1 .LBB0_70
	s_add_i32 s44, s42, s48
	s_cmp_lt_i32 s44, 0x800
	s_cbranch_scc1 .Lpt_1
	s_cmp_ge_i32 s44, 0xe580
	s_cbranch_scc1 .Lpt_1
	s_add_i32 s44, s44, 0xdd80

; #define LAS __attribute__((address_space(3)))
; #define LDS_WAIT() asm volatile("s_waitcnt lgkmcnt(0)" ::: "memory")
; __device__ __forceinline__ unsigned pk_fp8x4(float a, float b, float c, float d) { int p = __builtin_amdgcn_cvt_pk_fp8_f32(sat8(a), sat8(b), 0, false); p = __builtin_amdgcn_cvt_pk_fp8_f32(sat8(c), sat8(d), p, true); return (unsigned)p; }
; __device__ __forceinline__ void tr_finish(const TrDesc& d, f32x4 (&v)[16], LAS float* scr, int lane) {
;     ...
;     const int d0 = d.rope ? 8 * (q4 & 7) + (q4 >> 3) : 4 * q4, ds = d.rope ? 2 : 1;
;     { LAS float* rp = scr + kk * 65 + d0;
; #pragma unroll
;         for (int i = 0; i < 16; ++i) { rp[4 * i * 65] = v[i][0]; rp[4 * i * 65 + ds] = v[i][1]; rp[4 * i * 65 + 2 * ds] = v[i][2]; rp[4 * i * 65 + 3 * ds] = v[i][3]; } }
;     LDS_WAIT(); asm volatile("" ::: "memory");
;     if (d.f8) {
;         const int c = lane & 3, nl = lane >> 2; const LAS float* sp = scr + (16 * c) * 65 + nl; unsigned char* dp = d.dst + (size_t)nl * d.K + 16 * c;
; #pragma unroll
;         for (int j = 0; j < 4; ++j) { u32x4 o;
;             o.x = pk_fp8x4(sp[0 * 65 + 16 * j] * 32.0f, sp[1 * 65 + 16 * j] * 32.0f, sp[2 * 65 + 16 * j] * 32.0f, sp[3 * 65 + 16 * j] * 32.0f);
;             o.y = pk_fp8x4(sp[4 * 65 + 16 * j] * 32.0f, sp[5 * 65 + 16 * j] * 32.0f, sp[6 * 65 + 16 * j] * 32.0f, sp[7 * 65 + 16 * j] * 32.0f);
;             o.z = pk_fp8x4(sp[8 * 65 + 16 * j] * 32.0f, sp[9 * 65 + 16 * j] * 32.0f, sp[10 * 65 + 16 * j] * 32.0f, sp[11 * 65 + 16 * j] * 32.0f);
;             o.w = pk_fp8x4(sp[12 * 65 + 16 * j] * 32.0f, sp[13 * 65 + 16 * j] * 32.0f, sp[14 * 65 + 16 * j] * 32.0f, sp[15 * 65 + 16 * j] * 32.0f);
.LBB0_108:
	s_or_b64 exec, exec, s[22:23]
	s_cmp_eq_u32 s43, 0
	s_cselect_b64 vcc, -1, 0
	s_cmp_lg_u32 s43, 0
	s_cselect_b64 s[22:23], -1, 0
	v_cndmask_b32_e64 v2, 0, 1, s[22:23]
	s_and_b64 s[22:23], s[22:23], exec
	v_cndmask_b32_e32 v0, v140, v136, vcc
	s_cselect_b32 s0, 2, 1
	v_lshl_add_u32 v0, v0, 2, v141
	s_lshl_b32 s3, s0, 2
	v_add_u32_e32 v3, s3, v0
	v_lshlrev_b32_e64 v2, v2, 3
	s_waitcnt vmcnt(15)
	ds_write_b32 v3, v5
	v_lshl_add_u32 v3, s0, 3, v0
	v_lshl_add_u32 v2, v2, 2, v0
	v_subrev_u32_e32 v146, s3, v3
	ds_write_b32 v0, v4
	ds_write_b32 v3, v6
	ds_write_b32 v2, v7
	s_waitcnt vmcnt(14)
	ds_write_b32 v0, v8 offset:1040
	ds_write_b32 v146, v9 offset:1040
	ds_write_b32 v3, v10 offset:1040
	ds_write_b32 v2, v11 offset:1040
	s_waitcnt vmcnt(13)
	ds_write_b32 v0, v12 offset:2080
	ds_write_b32 v146, v13 offset:2080
	ds_write_b32 v3, v14 offset:2080
	ds_write_b32 v2, v15 offset:2080
	s_waitcnt vmcnt(12)
	ds_write_b32 v0, v16 offset:3120
	ds_write_b32 v146, v17 offset:3120
	ds_write_b32 v3, v18 offset:3120
	ds_write_b32 v2, v19 offset:3120
	s_waitcnt vmcnt(11)
	ds_write_b32 v0, v20 offset:4160
	ds_write_b32 v146, v21 offset:4160
	ds_write_b32 v3, v22 offset:4160
	ds_write_b32 v2, v23 offset:4160
	s_waitcnt vmcnt(10)
	ds_write_b32 v0, v24 offset:5200
	ds_write_b32 v146, v25 offset:5200
	ds_write_b32 v3, v26 offset:5200
	ds_write_b32 v2, v27 offset:5200
	s_waitcnt vmcnt(9)
	ds_write_b32 v0, v28 offset:6240
	ds_write_b32 v146, v29 offset:6240
	ds_write_b32 v3, v30 offset:6240
	ds_write_b32 v2, v31 offset:6240
	s_waitcnt vmcnt(8)
	ds_write_b32 v0, v32 offset:7280
	ds_write_b32 v146, v33 offset:7280
	ds_write_b32 v3, v34 offset:7280
	ds_write_b32 v2, v35 offset:7280
	s_waitcnt vmcnt(7)
	ds_write_b32 v0, v36 offset:8320
	ds_write_b32 v146, v37 offset:8320
	ds_write_b32 v3, v38 offset:8320
	ds_write_b32 v2, v39 offset:8320
	s_waitcnt vmcnt(6)
	ds_write_b32 v0, v40 offset:9360
	ds_write_b32 v146, v41 offset:9360
	ds_write_b32 v3, v42 offset:9360
	ds_write_b32 v2, v43 offset:9360
	s_waitcnt vmcnt(5)
	ds_write_b32 v0, v44 offset:10400
	ds_write_b32 v146, v45 offset:10400
	ds_write_b32 v3, v46 offset:10400
	ds_write_b32 v2, v47 offset:10400
	s_waitcnt vmcnt(4)
	ds_write_b32 v0, v48 offset:11440
	ds_write_b32 v146, v49 offset:11440
	ds_write_b32 v3, v50 offset:11440
	ds_write_b32 v2, v51 offset:11440
	s_waitcnt vmcnt(3)
	ds_write_b32 v0, v52 offset:12480
	ds_write_b32 v146, v53 offset:12480
	ds_write_b32 v3, v54 offset:12480
	ds_write_b32 v2, v55 offset:12480
	s_waitcnt vmcnt(2)
	ds_write_b32 v0, v56 offset:13520
	ds_write_b32 v146, v57 offset:13520
	ds_write_b32 v3, v58 offset:13520
	ds_write_b32 v2, v59 offset:13520
	s_waitcnt vmcnt(1)
	ds_write_b32 v0, v60 offset:14560
	ds_write_b32 v146, v61 offset:14560
	ds_write_b32 v3, v62 offset:14560
	ds_write_b32 v2, v63 offset:14560
	s_waitcnt vmcnt(0)
	ds_write_b32 v0, v64 offset:15600
	ds_write_b32 v146, v65 offset:15600
	ds_write_b32 v3, v66 offset:15600
	ds_write_b32 v2, v67 offset:15600
	s_waitcnt lgkmcnt(0)
	ds_read2_b32 v[2:3], v142 offset1:16
	ds_read2_b32 v[148:149], v142 offset0:65 offset1:81
	ds_read2_b32 v[154:155], v142 offset0:130 offset1:146
	ds_read2_b32 v[156:157], v142 offset0:195 offset1:211
	v_mov_b32_e32 v150, 0
	s_waitcnt lgkmcnt(3)
	v_mul_f32_e32 v0, 0x42000000, v2
	s_waitcnt lgkmcnt(2)
	v_mul_f32_e32 v2, 0x42000000, v148
	v_med3_f32 v0, v0, s41, v143
	s_waitcnt lgkmcnt(0)
	v_mul_f32_e32 v147, 0x42000000, v156
	v_med3_f32 v2, v2, s41, v143
	v_cvt_pk_fp8_f32 v150, v0, v2
	v_med3_f32 v2, v147, s41, v143
	v_add_u32_e32 v147, 0x400, v142
	ds_read2_b32 v[160:161], v147 offset0:4 offset1:20
	ds_read2_b32 v[162:163], v147 offset0:69 offset1:85
	ds_read2_b32 v[164:165], v147 offset0:134 offset1:150
	ds_read2_b32 v[166:167], v147 offset0:199 offset1:215
	v_mul_f32_e32 v146, 0x42000000, v154
	v_med3_f32 v0, v146, s41, v143
	v_cvt_pk_fp8_f32 v150, v0, v2 op_sel:[0,0,1]
	s_waitcnt lgkmcnt(3)
	v_mul_f32_e32 v0, 0x42000000, v160
	s_waitcnt lgkmcnt(2)
	v_mul_f32_e32 v2, 0x42000000, v162
	s_waitcnt lgkmcnt(0)
	v_mul_f32_e32 v148, 0x42000000, v166
	v_med3_f32 v0, v0, s41, v143
	v_med3_f32 v2, v2, s41, v143
	v_mov_b32_e32 v151, 0
	v_cvt_pk_fp8_f32 v151, v0, v2
	v_med3_f32 v2, v148, s41, v143
	v_add_u32_e32 v148, 0x800, v142
	ds_read2_b32 v[168:169], v148 offset0:8 offset1:24
	ds_read2_b32 v[170:171], v148 offset0:73 offset1:89
	ds_read2_b32 v[172:173], v148 offset0:138 offset1:154
	ds_read2_b32 v[174:175], v148 offset0:203 offset1:219
	v_mul_f32_e32 v146, 0x42000000, v164
	v_med3_f32 v0, v146, s41, v143
	v_cvt_pk_fp8_f32 v151, v0, v2 op_sel:[0,0,1]
	s_waitcnt lgkmcnt(3)
	v_mul_f32_e32 v0, 0x42000000, v168
	s_waitcnt lgkmcnt(2)
	v_mul_f32_e32 v2, 0x42000000, v170
	s_waitcnt lgkmcnt(1)
	v_mul_f32_e32 v146, 0x42000000, v172
	v_med3_f32 v0, v0, s41, v143
	v_med3_f32 v2, v2, s41, v143
	v_mov_b32_e32 v152, 0
	v_cvt_pk_fp8_f32 v152, v0, v2
	v_med3_f32 v0, v146, s41, v143
	v_add_u32_e32 v146, 0xc00, v142
	ds_read2_b32 v[176:177], v146 offset0:12 offset1:28
	ds_read2_b32 v[178:179], v146 offset0:77 offset1:93
	ds_read2_b32 v[180:181], v146 offset0:142 offset1:158
	s_waitcnt lgkmcnt(3)
	v_mul_f32_e32 v153, 0x42000000, v174
	v_med3_f32 v2, v153, s41, v143
	ds_read2_b32 v[182:183], v146 offset0:207 offset1:223
	v_cvt_pk_fp8_f32 v152, v0, v2 op_sel:[0,0,1]
	s_waitcnt lgkmcnt(3)
	v_mul_f32_e32 v0, 0x42000000, v176
	s_waitcnt lgkmcnt(2)
	v_mul_f32_e32 v2, 0x42000000, v178
	v_med3_f32 v0, v0, s41, v143
	v_med3_f32 v2, v2, s41, v143
	v_mov_b32_e32 v153, 0
	v_cvt_pk_fp8_f32 v153, v0, v2
	s_waitcnt lgkmcnt(1)
	v_mul_f32_e32 v154, 0x42000000, v180
	s_waitcnt lgkmcnt(0)
; #define LAS __attribute__((address_space(3)))
; #define GAS __attribute__((address_space(1)))
; __device__ __forceinline__ unsigned pk_fp8x4(float a, float b, float c, float d) { int p = __builtin_amdgcn_cvt_pk_fp8_f32(sat8(a), sat8(b), 0, false); p = __builtin_amdgcn_cvt_pk_fp8_f32(sat8(c), sat8(d), p, true); return (unsigned)p; }
; __device__ __forceinline__ void tr_finish(const TrDesc& d, f32x4 (&v)[16], LAS float* scr, int lane) {
;     ...
;         const int c = lane & 3, nl = lane >> 2; const LAS float* sp = scr + (16 * c) * 65 + nl; unsigned char* dp = d.dst + (size_t)nl * d.K + 16 * c;
; #pragma unroll
;         for (int j = 0; j < 4; ++j) { u32x4 o;
;             o.x = pk_fp8x4(sp[0 * 65 + 16 * j] * 32.0f, sp[1 * 65 + 16 * j] * 32.0f, sp[2 * 65 + 16 * j] * 32.0f, sp[3 * 65 + 16 * j] * 32.0f);
;             o.y = pk_fp8x4(sp[4 * 65 + 16 * j] * 32.0f, sp[5 * 65 + 16 * j] * 32.0f, sp[6 * 65 + 16 * j] * 32.0f, sp[7 * 65 + 16 * j] * 32.0f);
;             o.z = pk_fp8x4(sp[8 * 65 + 16 * j] * 32.0f, sp[9 * 65 + 16 * j] * 32.0f, sp[10 * 65 + 16 * j] * 32.0f, sp[11 * 65 + 16 * j] * 32.0f);
;             o.w = pk_fp8x4(sp[12 * 65 + 16 * j] * 32.0f, sp[13 * 65 + 16 * j] * 32.0f, sp[14 * 65 + 16 * j] * 32.0f, sp[15 * 65 + 16 * j] * 32.0f);
;             *(GAS u32x4*)(dp + (size_t)(16 * j) * d.K) = o; }
;     ...
;         while (it < NIT) {
;             const int itB = it + NGW;
;             if (itB < NIT) { dB = decode(NIT - 1 - itB); tr_load(dB, vB); }
;             tr_finish(dA, vA, scr, lane);
;             if (itB >= NIT) break;
;             const int itA = itB + NGW;
;             if (itA < NIT) { dA = decode(NIT - 1 - itA); tr_load(dA, vA); }
;             tr_finish(dB, vB, scr, lane);
;             it = itA;
	v_mul_f32_e32 v0, 0x42000000, v182
	v_med3_f32 v2, v154, s41, v143
	v_med3_f32 v0, v0, s41, v143
	v_cvt_pk_fp8_f32 v153, v2, v0 op_sel:[0,0,1]
	v_mov_b64_e32 v[158:159], s[16:17]
	v_mad_i64_i32 v[158:159], s[22:23], s2, v132, v[158:159]
	v_lshl_add_u64 v[158:159], v[158:159], 0, v[134:135]
	v_mul_f32_e32 v0, 0x42000000, v3
	v_mul_f32_e32 v2, 0x42000000, v149
	global_store_dwordx4 v[158:159], v[150:153], off
	v_med3_f32 v0, v0, s41, v143
	v_med3_f32 v2, v2, s41, v143
	v_mov_b32_e32 v150, 0
	v_cvt_pk_fp8_f32 v150, v0, v2
	v_mul_f32_e32 v3, 0x42000000, v155
	v_mul_f32_e32 v0, 0x42000000, v157
	v_med3_f32 v2, v3, s41, v143
	v_med3_f32 v0, v0, s41, v143
	v_cvt_pk_fp8_f32 v150, v2, v0 op_sel:[0,0,1]
	v_mul_f32_e32 v0, 0x42000000, v161
	v_mul_f32_e32 v2, 0x42000000, v163
	v_med3_f32 v0, v0, s41, v143
	v_med3_f32 v2, v2, s41, v143
	v_mov_b32_e32 v151, 0
	v_cvt_pk_fp8_f32 v151, v0, v2
	v_mul_f32_e32 v3, 0x42000000, v165
	v_mul_f32_e32 v0, 0x42000000, v167
	v_med3_f32 v2, v3, s41, v143
	v_med3_f32 v0, v0, s41, v143
	v_cvt_pk_fp8_f32 v151, v2, v0 op_sel:[0,0,1]
	v_mul_f32_e32 v0, 0x42000000, v169
	v_mul_f32_e32 v2, 0x42000000, v171
	v_med3_f32 v0, v0, s41, v143
	v_med3_f32 v2, v2, s41, v143
	v_mov_b32_e32 v152, 0
	v_cvt_pk_fp8_f32 v152, v0, v2
	v_mul_f32_e32 v3, 0x42000000, v173
	v_mul_f32_e32 v0, 0x42000000, v175
	v_med3_f32 v2, v3, s41, v143
	v_med3_f32 v0, v0, s41, v143
	v_cvt_pk_fp8_f32 v152, v2, v0 op_sel:[0,0,1]
	v_mul_f32_e32 v0, 0x42000000, v177
	v_mul_f32_e32 v2, 0x42000000, v179
	v_med3_f32 v0, v0, s41, v143
	v_med3_f32 v2, v2, s41, v143
	v_mov_b32_e32 v153, 0
	v_cvt_pk_fp8_f32 v153, v0, v2
	s_ashr_i32 s3, s2, 31
	v_mul_f32_e32 v3, 0x42000000, v181
	v_mul_f32_e32 v0, 0x42000000, v183
	v_med3_f32 v2, v3, s41, v143
	v_med3_f32 v0, v0, s41, v143
	s_lshl_b64 s[22:23], s[2:3], 4
	v_cvt_pk_fp8_f32 v153, v2, v0 op_sel:[0,0,1]
	v_lshl_add_u64 v[2:3], v[158:159], 0, s[22:23]
	ds_read2_b32 v[154:155], v142 offset0:32 offset1:48
	ds_read2_b32 v[156:157], v142 offset0:97 offset1:113
	ds_read2_b32 v[158:159], v142 offset0:162 offset1:178
	ds_read2_b32 v[160:161], v142 offset0:227 offset1:243
	s_andn2_b64 vcc, exec, s[20:21]
	s_waitcnt lgkmcnt(3)
	v_mul_f32_e32 v0, 0x42000000, v154
	s_waitcnt lgkmcnt(2)
	v_mul_f32_e32 v149, 0x42000000, v156
	global_store_dwordx4 v[2:3], v[150:153], off
	v_med3_f32 v0, v0, s41, v143
	v_med3_f32 v149, v149, s41, v143
	v_mov_b32_e32 v150, 0
	v_cvt_pk_fp8_f32 v150, v0, v149
	ds_read2_b32 v[162:163], v147 offset0:36 offset1:52
	ds_read2_b32 v[164:165], v147 offset0:101 offset1:117
	ds_read2_b32 v[166:167], v147 offset0:166 offset1:182
	ds_read2_b32 v[168:169], v147 offset0:231 offset1:247
	s_waitcnt lgkmcnt(5)
	v_mul_f32_e32 v151, 0x42000000, v158
	s_waitcnt lgkmcnt(4)
	v_mul_f32_e32 v152, 0x42000000, v160
	v_med3_f32 v0, v151, s41, v143
	v_med3_f32 v149, v152, s41, v143
	v_cvt_pk_fp8_f32 v150, v0, v149 op_sel:[0,0,1]
	s_waitcnt lgkmcnt(3)
	v_mul_f32_e32 v0, 0x42000000, v162
	s_waitcnt lgkmcnt(2)
	v_mul_f32_e32 v149, 0x42000000, v164
	v_med3_f32 v0, v0, s41, v143
	v_med3_f32 v149, v149, s41, v143
	v_mov_b32_e32 v151, 0
	v_cvt_pk_fp8_f32 v151, v0, v149
	ds_read2_b32 v[170:171], v148 offset0:40 offset1:56
	ds_read2_b32 v[172:173], v148 offset0:105 offset1:121
	ds_read2_b32 v[174:175], v148 offset0:170 offset1:186
	ds_read2_b32 v[176:177], v148 offset0:235 offset1:251
	s_waitcnt lgkmcnt(5)
	v_mul_f32_e32 v152, 0x42000000, v166
	s_waitcnt lgkmcnt(4)
	v_mul_f32_e32 v153, 0x42000000, v168
	v_med3_f32 v0, v152, s41, v143
	v_med3_f32 v149, v153, s41, v143
	v_cvt_pk_fp8_f32 v151, v0, v149 op_sel:[0,0,1]
	s_waitcnt lgkmcnt(3)
	v_mul_f32_e32 v0, 0x42000000, v170
	s_waitcnt lgkmcnt(2)
	v_mul_f32_e32 v149, 0x42000000, v172
	v_med3_f32 v0, v0, s41, v143
	v_med3_f32 v149, v149, s41, v143
	v_mov_b32_e32 v152, 0
	v_cvt_pk_fp8_f32 v152, v0, v149
	ds_read2_b32 v[178:179], v146 offset0:44 offset1:60
	ds_read2_b32 v[180:181], v146 offset0:109 offset1:125
	ds_read2_b32 v[182:183], v146 offset0:174 offset1:190
	s_waitcnt lgkmcnt(4)
	v_mul_f32_e32 v153, 0x42000000, v174
	s_waitcnt lgkmcnt(3)
	v_mul_f32_e32 v154, 0x42000000, v176
	v_med3_f32 v0, v153, s41, v143
	v_med3_f32 v149, v154, s41, v143
	ds_read2_b32 v[184:185], v146 offset0:239 offset1:255
	v_cvt_pk_fp8_f32 v152, v0, v149 op_sel:[0,0,1]
	s_waitcnt lgkmcnt(3)
	v_mul_f32_e32 v0, 0x42000000, v178
	s_waitcnt lgkmcnt(2)
	v_mul_f32_e32 v149, 0x42000000, v180
	v_med3_f32 v0, v0, s41, v143
	v_med3_f32 v149, v149, s41, v143
	v_mov_b32_e32 v153, 0
	v_cvt_pk_fp8_f32 v153, v0, v149
	s_waitcnt lgkmcnt(1)
	v_mul_f32_e32 v154, 0x42000000, v182
	s_waitcnt lgkmcnt(0)
	v_mul_f32_e32 v0, 0x42000000, v184
	v_med3_f32 v149, v154, s41, v143
	v_med3_f32 v0, v0, s41, v143
	v_cvt_pk_fp8_f32 v153, v149, v0 op_sel:[0,0,1]
	v_mul_f32_e32 v0, 0x42000000, v155
	v_mul_f32_e32 v149, 0x42000000, v157
	v_med3_f32 v0, v0, s41, v143
	v_med3_f32 v149, v149, s41, v143
	v_mov_b32_e32 v154, 0
	v_cvt_pk_fp8_f32 v154, v0, v149
	v_mul_f32_e32 v155, 0x42000000, v159
	v_mul_f32_e32 v0, 0x42000000, v161
	v_med3_f32 v149, v155, s41, v143
	v_med3_f32 v0, v0, s41, v143
	v_cvt_pk_fp8_f32 v154, v149, v0 op_sel:[0,0,1]
	v_mul_f32_e32 v0, 0x42000000, v163
	v_mul_f32_e32 v149, 0x42000000, v165
	v_med3_f32 v0, v0, s41, v143
	v_med3_f32 v149, v149, s41, v143
	v_mov_b32_e32 v155, 0
	v_cvt_pk_fp8_f32 v155, v0, v149
	v_mul_f32_e32 v156, 0x42000000, v167
	v_mul_f32_e32 v0, 0x42000000, v169
	v_med3_f32 v149, v156, s41, v143
	v_med3_f32 v0, v0, s41, v143
	v_cvt_pk_fp8_f32 v155, v149, v0 op_sel:[0,0,1]
	v_mul_f32_e32 v0, 0x42000000, v171
	v_mul_f32_e32 v149, 0x42000000, v173
	v_med3_f32 v0, v0, s41, v143
	v_med3_f32 v149, v149, s41, v143
	v_mov_b32_e32 v156, 0
	v_cvt_pk_fp8_f32 v156, v0, v149
	v_mul_f32_e32 v157, 0x42000000, v175
	v_mul_f32_e32 v0, 0x42000000, v177
	v_med3_f32 v149, v157, s41, v143
	v_med3_f32 v0, v0, s41, v143
	v_cvt_pk_fp8_f32 v156, v149, v0 op_sel:[0,0,1]
	v_mul_f32_e32 v0, 0x42000000, v179
	v_mul_f32_e32 v149, 0x42000000, v181
	v_med3_f32 v0, v0, s41, v143
	v_med3_f32 v149, v149, s41, v143
	v_mov_b32_e32 v157, 0
	v_cvt_pk_fp8_f32 v157, v0, v149
	v_mul_f32_e32 v158, 0x42000000, v183
	v_mul_f32_e32 v0, 0x42000000, v185
	v_med3_f32 v149, v158, s41, v143
	v_med3_f32 v0, v0, s41, v143
	v_cvt_pk_fp8_f32 v157, v149, v0 op_sel:[0,0,1]
	v_lshl_add_u64 v[2:3], v[2:3], 0, s[22:23]
	global_store_dwordx4 v[2:3], v[150:153], off
	v_lshl_add_u64 v[2:3], v[2:3], 0, s[22:23]
	global_store_dwordx4 v[2:3], v[154:157], off
	s_waitcnt lgkmcnt(0)
	s_cbranch_vccnz .LBB0_71
	s_add_i32 s42, s44, s48
	s_cmp_lt_i32 s42, 0x800
	s_cbranch_scc1 .Lpt_2
	s_cmp_ge_i32 s42, 0xe580
	s_cbranch_scc1 .Lpt_2
	s_add_i32 s42, s42, 0xdd80

; #define LAS __attribute__((address_space(3)))
; #define FRESH_TID() do { ap = fresh_args(); ws = ap->ws; unsigned m1_ = ~0u; asm volatile("" : "+s"(m1_)); lane = (int)__builtin_amdgcn_mbcnt_hi(m1_, __builtin_amdgcn_mbcnt_lo(m1_, 0u)); asm volatile("" : "+v"(lane)); wave = wave0; tid = wave0 * 64 + lane; } while (0)
; __device__ __forceinline__ void moe_table_build(LAS unsigned char* lds, const unsigned* cnt, int tid) {
;     if (tid < NE) { const int n = (int)__hip_atomic_load(cnt + 64 * tid, RLX_AGENT); ((LAS int*)(lds + MOE_TAB_OFF))[16 + tid] = n; }
;     __syncthreads();
;     if (tid == 0) { int acc = 0; for (int e = 0; e < NE; ++e) { acc += (((LAS int*)(lds + MOE_TAB_OFF))[16 + e] + 255) >> 8; ((LAS int*)(lds + MOE_TAB_OFF))[e] = acc; } }
;     __syncthreads();
; template <unsigned MASK, bool ONE>
; __global__ void __launch_bounds__(NTHREADS, 2) fwd_kernel(Args a_unused) {
;     ...
;         if (IN(P + 9, 10)) { FRESH_TID();
;             pg8::moe_table_build(lds, cntl, tid);
;             pg8::MoeOrder S; S.init(lds, 8, G, bx); pg8::RowsContig AM; pg8::EpiPlainS E{Y, pg8::W8_INV};
.LBB0_1006:
	s_or_b64 exec, exec, s[0:1]
	v_readlane_b32 s101, v255, 17
	s_movk_i32 s100, 0x100
	s_cmp_eq_u32 s101, 0
	s_cselect_b32 s100, 0xa0, s100
	s_cselect_b32 s101, 96, 0
	v_readlane_b32 s0, v253, 0
	v_readlane_b32 s1, v253, 1
	s_waitcnt lgkmcnt(0)
	s_barrier
	s_load_dwordx2 s[6:7], s[0:1], 0xa0
	s_mov_b32 s0, s38
	s_nop 0
	v_mbcnt_lo_u32_b32 v0, s0, 0
	v_mbcnt_hi_u32_b32 v0, s0, v0
	s_nop 0
	v_add_u32_e32 v1, s78, v0
	v_cmp_gt_i32_e32 vcc, 16, v1
	s_and_saveexec_b64 s[0:1], vcc
	s_cbranch_execz .LBB0_1008
	s_lshl_b64 s[2:3], s[96:97], 2
	s_waitcnt lgkmcnt(0)
	s_add_u32 s2, s6, s2
	v_lshlrev_b32_e32 v2, 6, v1
	s_addc_u32 s3, s7, s3
	v_ashrrev_i32_e32 v3, 31, v2
	v_lshl_add_u64 v[2:3], v[2:3], 2, s[2:3]
	v_add_co_u32_e32 v2, vcc, 0x10000, v2
	v_readlane_b32 s2, v255, 23
	s_nop 0
	v_addc_co_u32_e32 v3, vcc, 0, v3, vcc
	global_load_dword v2, v[2:3], off sc1
	v_lshl_add_u32 v3, v1, 2, s2
	s_waitcnt vmcnt(0)
	ds_write_b32 v3, v2 offset:64
.LBB0_1008:
	s_or_b64 exec, exec, s[0:1]
	v_cmp_eq_u32_e32 vcc, 0, v1
	s_waitcnt lgkmcnt(0)
	s_barrier
	s_and_saveexec_b64 s[0:1], vcc
	v_readlane_b32 s67, v255, 23
	v_readlane_b32 s68, v255, 24
	v_readlane_b32 s69, v255, 25
	v_readlane_b32 s71, v255, 26
	s_cbranch_execz .LBB0_1010
	v_readlane_b32 s2, v254, 54
	v_mov_b32_e32 v6, s67
	s_nop 0
	v_mov_b32_e32 v2, s2
	ds_read_b128 v[2:5], v2
	v_readlane_b32 s2, v254, 55
	s_waitcnt lgkmcnt(0)
	v_add_u32_e32 v2, 0xff, v2
	v_add_u32_e32 v3, 0xff, v3
	v_ashrrev_i32_e32 v2, 8, v2
	v_ashrrev_i32_e32 v3, 8, v3
	v_add_u32_e32 v4, 0xff, v4
	v_add_u32_e32 v3, v3, v2
	v_ashrrev_i32_e32 v4, 8, v4
	v_add_u32_e32 v5, 0xff, v5
	v_add_u32_e32 v4, v4, v3
	v_ashrrev_i32_e32 v5, 8, v5
	v_add_u32_e32 v5, v5, v4
	ds_write_b128 v6, v[2:5]
	v_mov_b32_e32 v2, s2
	ds_read_b128 v[6:9], v2
	v_readlane_b32 s2, v254, 56
	s_waitcnt lgkmcnt(0)
	v_add_u32_e32 v2, 0xff, v6
	v_ashrrev_i32_e32 v2, 8, v2
	v_add_u32_e32 v3, 0xff, v7
	v_add_u32_e32 v2, v2, v5
	v_ashrrev_i32_e32 v3, 8, v3
	v_add_u32_e32 v4, 0xff, v8
	v_add_u32_e32 v3, v3, v2
	v_ashrrev_i32_e32 v4, 8, v4
	v_add_u32_e32 v5, 0xff, v9
	v_add_u32_e32 v4, v4, v3
	v_ashrrev_i32_e32 v5, 8, v5
	v_add_u32_e32 v5, v5, v4
	v_mov_b32_e32 v6, s68
	ds_write_b128 v6, v[2:5]
	v_mov_b32_e32 v2, s2
	ds_read_b128 v[6:9], v2
	v_readlane_b32 s2, v254, 57
	s_waitcnt lgkmcnt(0)
	v_add_u32_e32 v2, 0xff, v6
	v_ashrrev_i32_e32 v2, 8, v2
	v_add_u32_e32 v3, 0xff, v7
	v_add_u32_e32 v2, v2, v5
	v_ashrrev_i32_e32 v3, 8, v3
	v_add_u32_e32 v4, 0xff, v8
	v_add_u32_e32 v3, v3, v2
	v_ashrrev_i32_e32 v4, 8, v4
	v_add_u32_e32 v5, 0xff, v9
	v_add_u32_e32 v4, v4, v3
	v_ashrrev_i32_e32 v5, 8, v5
	v_add_u32_e32 v5, v5, v4
	v_mov_b32_e32 v6, s69
	ds_write_b128 v6, v[2:5]
	v_mov_b32_e32 v2, s2
	ds_read_b128 v[6:9], v2
	s_waitcnt lgkmcnt(0)
	v_add_u32_e32 v2, 0xff, v6
	v_ashrrev_i32_e32 v2, 8, v2
	v_add_u32_e32 v3, 0xff, v7
	v_add_u32_e32 v2, v2, v5
	v_ashrrev_i32_e32 v3, 8, v3
	v_add_u32_e32 v4, 0xff, v8
	v_add_u32_e32 v3, v3, v2
	v_ashrrev_i32_e32 v4, 8, v4
	v_add_u32_e32 v5, 0xff, v9
	v_add_u32_e32 v4, v4, v3
	v_ashrrev_i32_e32 v5, 8, v5
	v_add_u32_e32 v5, v5, v4
	v_mov_b32_e32 v6, s71
	ds_write_b128 v6, v[2:5]
.LBB0_1010:
	s_or_b64 exec, exec, s[0:1]
	v_readlane_b32 s0, v254, 58
	s_waitcnt lgkmcnt(0)
	s_barrier
	v_mov_b32_e32 v2, s0
	ds_read_b32 v2, v2
	v_readlane_b32 s1, v253, 4
	v_readfirstlane_b32 s14, v1
	v_readlane_b32 s65, v255, 22
	s_movk_i32 s66, 0x179
	s_waitcnt lgkmcnt(0)
	v_readfirstlane_b32 s16, v2
	s_lshl_b32 s0, s16, 3
	s_cmp_eq_u32 s101, 0
	s_cbranch_scc1 .Lno_help10
	s_cmpk_lt_i32 s1, 0xa0
	s_cbranch_scc1 .Lno_help10
	s_mov_b32 s100, 0x800
	s_mov_b32 s101, 0x3cc0
	s_mov_b32 s62, 0x20600000
	s_mov_b32 s0, 1
	v_writelane_b32 v251, s0, 30
	s_movk_i32 s0, 96
	s_branch .Lhp_entry
